# grid barrier: the first and the 17th arriver of each XCD start an L2 write-back early so the last arriver's write-back finds less dirty data
# baseline (speedup 1.0000x reference)
; __device__ __forceinline__ unsigned xb_ld(unsigned* p)              { return __hip_atomic_load(p, __ATOMIC_RELAXED, __HIP_MEMORY_SCOPE_AGENT); }
; __device__ __forceinline__ unsigned xb_add(unsigned* p, unsigned v) { return __hip_atomic_fetch_add(p, v, __ATOMIC_RELAXED, __HIP_MEMORY_SCOPE_AGENT); }
; __device__ __forceinline__ unsigned xb_xcc_id() { return (unsigned)__builtin_amdgcn_s_getreg((3 << 11) | 20) & 0xFu; }
; #define XB_SPIN(cond, bar) do { unsigned _sp = 0; while (cond) { __builtin_amdgcn_s_sleep(1); \
;     if ((++_sp & 255u) == 0u) { if (xb_ld(&(bar)[XB_TMO])) break; if (_sp > XB_SPIN_CAP) { atomicAdd(&(bar)[XB_TMO], 1u); break; } } } } while (0)
; __device__ __forceinline__ void xcd_barrier(const XcdBarrier& b) {
;     ...
;         __builtin_amdgcn_s_waitcnt(0);
;         const unsigned bx = xb_xcc_id();
;         unsigned nloc = b.st[0], nx = b.st[1];
;         if (nloc == 0u) { xcd_barrier_complete(bar, bx, nloc, nx); b.st[0] = nloc; b.st[1] = nx; }
;         const unsigned old = xb_add(&bar[XB_XSUB(bx)], 1u);
;         const unsigned gen = old / nloc;
;         if (old + 1u == (gen + 1u) * nloc) {
;             __builtin_amdgcn_fence(__ATOMIC_RELEASE, "agent");
;             asm volatile("s_waitcnt vmcnt(0)" ::: "memory");
;             const unsigned og = xb_add(&bar[XB_TOP], 1u);
;             const unsigned tg = og / nx;
;             if (og + 1u == (tg + 1u) * nx) xb_add(&bar[XB_TOPGEN], 1u);
;             else XB_SPIN(xb_ld(&bar[XB_TOPGEN]) == tg, bar);
;             __builtin_amdgcn_fence(__ATOMIC_ACQUIRE, "agent");
;             xb_add(&bar[XB_XGEN(bx)], 1u);
.LBB0_237:
	s_mov_b32 s0, s93
	s_waitcnt lgkmcnt(0)
	s_barrier
	s_waitcnt vmcnt(0)
	s_barrier
	s_nop 0
	v_mbcnt_lo_u32_b32 v0, -1, s0
	v_mbcnt_hi_u32_b32 v0, -1, v0
	v_readlane_b32 s0, v254, 17
	s_nop 1
	v_cmp_eq_u32_e32 vcc, s0, v0
	s_and_saveexec_b64 s[30:31], vcc
	s_mov_b32 s73, 0x8000
	s_mov_b32 s92, 0xa000
	s_cbranch_execz .LBB0_281
	s_bitcmp1_b32 s100, 0
	s_cbranch_scc0 .Lgb0_orig
	v_readlane_b32 s40, v253, 53
	v_readlane_b32 s41, v253, 54
	s_getreg_b32 s0, hwreg(HW_REG_XCC_ID, 0, 4)
	v_mov_b32_e32 v1, 1
	s_and_b32 s0, s0, 15
	s_lshl_b32 s0, s0, 8
	s_addk_i32 s0, 0x1400
	v_mov_b32_e32 v0, s0
	s_waitcnt vmcnt(0) lgkmcnt(0)
	global_atomic_add v2, v0, v1, s[40:41] sc0
	s_waitcnt vmcnt(0)
	v_readfirstlane_b32 s0, v2
	s_lshr_b32 s1, s0, 5
	s_and_b32 s0, s0, 31
	s_add_i32 s1, s1, 1
	s_lshl_b32 s1, s1, 3
	s_cmp_lg_u32 s0, 31
	s_cbranch_scc0 .Lgb0_last
	s_and_b32 s0, s0, 15
	s_cmp_lg_u32 s0, 0
	s_cbranch_scc1 .Lgb0_poll
	buffer_wbl2 sc1
	s_branch .Lgb0_poll
.Lgb0_last:
	buffer_wbl2 sc1
	s_waitcnt vmcnt(0)
	v_add_u32_e32 v0, 0x1000, v0
	global_atomic_add v0, v1, s[40:41]
	v_mov_b32_e32 v0, 0x3400
	global_atomic_add v2, v0, v1, s[40:41] sc0
	s_waitcnt vmcnt(0)
	v_readfirstlane_b32 s0, v2
	s_add_i32 s0, s0, 1
	s_cmp_lg_u32 s0, s1
	s_cbranch_scc1 .Lgb0_poll
	v_mov_b32_e32 v0, 0x3500
	global_atomic_add v0, v1, s[40:41]
	s_branch .Lgb0_done

; __device__ __forceinline__ unsigned xb_ld(unsigned* p)              { return __hip_atomic_load(p, __ATOMIC_RELAXED, __HIP_MEMORY_SCOPE_AGENT); }
; __device__ __forceinline__ unsigned xb_add(unsigned* p, unsigned v) { return __hip_atomic_fetch_add(p, v, __ATOMIC_RELAXED, __HIP_MEMORY_SCOPE_AGENT); }
; __device__ __forceinline__ unsigned xb_xcc_id() { return (unsigned)__builtin_amdgcn_s_getreg((3 << 11) | 20) & 0xFu; }
; #define XB_SPIN(cond, bar) do { unsigned _sp = 0; while (cond) { __builtin_amdgcn_s_sleep(1); \
;     if ((++_sp & 255u) == 0u) { if (xb_ld(&(bar)[XB_TMO])) break; if (_sp > XB_SPIN_CAP) { atomicAdd(&(bar)[XB_TMO], 1u); break; } } } } while (0)
; __device__ __forceinline__ void xcd_barrier(const XcdBarrier& b) {
;     ...
;         __builtin_amdgcn_s_waitcnt(0);
;         const unsigned bx = xb_xcc_id();
;         unsigned nloc = b.st[0], nx = b.st[1];
;         if (nloc == 0u) { xcd_barrier_complete(bar, bx, nloc, nx); b.st[0] = nloc; b.st[1] = nx; }
;         const unsigned old = xb_add(&bar[XB_XSUB(bx)], 1u);
;         const unsigned gen = old / nloc;
;         if (old + 1u == (gen + 1u) * nloc) {
;             __builtin_amdgcn_fence(__ATOMIC_RELEASE, "agent");
;             asm volatile("s_waitcnt vmcnt(0)" ::: "memory");
;             const unsigned og = xb_add(&bar[XB_TOP], 1u);
;             const unsigned tg = og / nx;
;             if (og + 1u == (tg + 1u) * nx) xb_add(&bar[XB_TOPGEN], 1u);
;             else XB_SPIN(xb_ld(&bar[XB_TOPGEN]) == tg, bar);
;             __builtin_amdgcn_fence(__ATOMIC_ACQUIRE, "agent");
;             xb_add(&bar[XB_XGEN(bx)], 1u);
.LBB0_300:
	s_mov_b32 s0, s93
	s_waitcnt vmcnt(0)
	s_waitcnt lgkmcnt(0)
	s_barrier
	s_waitcnt vmcnt(0)
	v_mbcnt_lo_u32_b32 v0, -1, s0
	v_mbcnt_hi_u32_b32 v0, -1, v0
	v_readlane_b32 s0, v254, 17
	s_nop 1
	v_cmp_eq_u32_e32 vcc, s0, v0
	s_and_saveexec_b64 s[0:1], vcc
	s_cbranch_execz .LBB0_344
	s_bitcmp1_b32 s100, 0
	s_cbranch_scc0 .Lgb1_orig
	v_readlane_b32 s40, v253, 53
	v_readlane_b32 s41, v253, 54
	s_getreg_b32 s2, hwreg(HW_REG_XCC_ID, 0, 4)
	v_mov_b32_e32 v1, 1
	s_and_b32 s2, s2, 15
	s_lshl_b32 s2, s2, 8
	s_addk_i32 s2, 0x1400
	v_mov_b32_e32 v0, s2
	s_waitcnt vmcnt(0) lgkmcnt(0)
	global_atomic_add v2, v0, v1, s[40:41] sc0
	s_waitcnt vmcnt(0)
	v_readfirstlane_b32 s2, v2
	s_lshr_b32 s3, s2, 5
	s_and_b32 s2, s2, 31
	s_add_i32 s3, s3, 1
	s_lshl_b32 s3, s3, 3
	s_cmp_lg_u32 s2, 31
	s_cbranch_scc0 .Lgb1_last
	s_and_b32 s2, s2, 15
	s_cmp_lg_u32 s2, 0
	s_cbranch_scc1 .Lgb1_poll
	buffer_wbl2 sc1
	s_branch .Lgb1_poll
.Lgb1_last:
	buffer_wbl2 sc1
	s_waitcnt vmcnt(0)
	v_add_u32_e32 v0, 0x1000, v0
	global_atomic_add v0, v1, s[40:41]
	v_mov_b32_e32 v0, 0x3400
	global_atomic_add v2, v0, v1, s[40:41] sc0
	s_waitcnt vmcnt(0)
	v_readfirstlane_b32 s2, v2
	s_add_i32 s2, s2, 1
	s_cmp_lg_u32 s2, s3
	s_cbranch_scc1 .Lgb1_poll
	v_mov_b32_e32 v0, 0x3500
	global_atomic_add v0, v1, s[40:41]
	s_branch .Lgb1_done

; __device__ __forceinline__ unsigned xb_ld(unsigned* p)              { return __hip_atomic_load(p, __ATOMIC_RELAXED, __HIP_MEMORY_SCOPE_AGENT); }
; __device__ __forceinline__ unsigned xb_add(unsigned* p, unsigned v) { return __hip_atomic_fetch_add(p, v, __ATOMIC_RELAXED, __HIP_MEMORY_SCOPE_AGENT); }
; __device__ __forceinline__ unsigned xb_xcc_id() { return (unsigned)__builtin_amdgcn_s_getreg((3 << 11) | 20) & 0xFu; }
; #define XB_SPIN(cond, bar) do { unsigned _sp = 0; while (cond) { __builtin_amdgcn_s_sleep(1); \
;     if ((++_sp & 255u) == 0u) { if (xb_ld(&(bar)[XB_TMO])) break; if (_sp > XB_SPIN_CAP) { atomicAdd(&(bar)[XB_TMO], 1u); break; } } } } while (0)
; __device__ __forceinline__ void xcd_barrier(const XcdBarrier& b) {
;     ...
;         __builtin_amdgcn_s_waitcnt(0);
;         const unsigned bx = xb_xcc_id();
;         unsigned nloc = b.st[0], nx = b.st[1];
;         if (nloc == 0u) { xcd_barrier_complete(bar, bx, nloc, nx); b.st[0] = nloc; b.st[1] = nx; }
;         const unsigned old = xb_add(&bar[XB_XSUB(bx)], 1u);
;         const unsigned gen = old / nloc;
;         if (old + 1u == (gen + 1u) * nloc) {
;             __builtin_amdgcn_fence(__ATOMIC_RELEASE, "agent");
;             asm volatile("s_waitcnt vmcnt(0)" ::: "memory");
;             const unsigned og = xb_add(&bar[XB_TOP], 1u);
;             const unsigned tg = og / nx;
;             if (og + 1u == (tg + 1u) * nx) xb_add(&bar[XB_TOPGEN], 1u);
;             else XB_SPIN(xb_ld(&bar[XB_TOPGEN]) == tg, bar);
;             __builtin_amdgcn_fence(__ATOMIC_ACQUIRE, "agent");
;             xb_add(&bar[XB_XGEN(bx)], 1u);
.LBB0_462:
	s_mov_b32 s0, s93
	s_waitcnt vmcnt(0)
	s_waitcnt lgkmcnt(0)
	s_barrier
	s_nop 0
	v_mbcnt_lo_u32_b32 v0, -1, s0
	v_mbcnt_hi_u32_b32 v0, -1, v0
	v_readlane_b32 s0, v254, 17
	s_nop 1
	v_cmp_eq_u32_e32 vcc, s0, v0
	s_and_saveexec_b64 s[0:1], vcc
	s_cbranch_execz .LBB0_506
	s_bitcmp1_b32 s100, 0
	s_cbranch_scc0 .Lgb2_orig
	v_readlane_b32 s36, v253, 53
	v_readlane_b32 s37, v253, 54
	s_getreg_b32 s2, hwreg(HW_REG_XCC_ID, 0, 4)
	v_mov_b32_e32 v1, 1
	s_and_b32 s2, s2, 15
	s_lshl_b32 s2, s2, 8
	s_addk_i32 s2, 0x1400
	v_mov_b32_e32 v0, s2
	s_waitcnt vmcnt(0) lgkmcnt(0)
	global_atomic_add v2, v0, v1, s[36:37] sc0
	s_waitcnt vmcnt(0)
	v_readfirstlane_b32 s2, v2
	s_lshr_b32 s3, s2, 5
	s_and_b32 s2, s2, 31
	s_add_i32 s3, s3, 1
	s_lshl_b32 s3, s3, 3
	s_cmp_lg_u32 s2, 31
	s_cbranch_scc0 .Lgb2_last
	s_and_b32 s2, s2, 15
	s_cmp_lg_u32 s2, 0
	s_cbranch_scc1 .Lgb2_poll
	buffer_wbl2 sc1
	s_branch .Lgb2_poll
.Lgb2_last:
	buffer_wbl2 sc1
	s_waitcnt vmcnt(0)
	v_add_u32_e32 v0, 0x1000, v0
	global_atomic_add v0, v1, s[36:37]
	v_mov_b32_e32 v0, 0x3400
	global_atomic_add v2, v0, v1, s[36:37] sc0
	s_waitcnt vmcnt(0)
	v_readfirstlane_b32 s2, v2
	s_add_i32 s2, s2, 1
	s_cmp_lg_u32 s2, s3
	s_cbranch_scc1 .Lgb2_poll
	v_mov_b32_e32 v0, 0x3500
	global_atomic_add v0, v1, s[36:37]
	s_branch .Lgb2_done

; __device__ __forceinline__ unsigned xb_ld(unsigned* p)              { return __hip_atomic_load(p, __ATOMIC_RELAXED, __HIP_MEMORY_SCOPE_AGENT); }
; __device__ __forceinline__ unsigned xb_add(unsigned* p, unsigned v) { return __hip_atomic_fetch_add(p, v, __ATOMIC_RELAXED, __HIP_MEMORY_SCOPE_AGENT); }
; __device__ __forceinline__ unsigned xb_xcc_id() { return (unsigned)__builtin_amdgcn_s_getreg((3 << 11) | 20) & 0xFu; }
; #define XB_SPIN(cond, bar) do { unsigned _sp = 0; while (cond) { __builtin_amdgcn_s_sleep(1); \
;     if ((++_sp & 255u) == 0u) { if (xb_ld(&(bar)[XB_TMO])) break; if (_sp > XB_SPIN_CAP) { atomicAdd(&(bar)[XB_TMO], 1u); break; } } } } while (0)
; __device__ __forceinline__ void xcd_barrier(const XcdBarrier& b) {
;     ...
;         __builtin_amdgcn_s_waitcnt(0);
;         const unsigned bx = xb_xcc_id();
;         unsigned nloc = b.st[0], nx = b.st[1];
;         if (nloc == 0u) { xcd_barrier_complete(bar, bx, nloc, nx); b.st[0] = nloc; b.st[1] = nx; }
;         const unsigned old = xb_add(&bar[XB_XSUB(bx)], 1u);
;         const unsigned gen = old / nloc;
;         if (old + 1u == (gen + 1u) * nloc) {
;             __builtin_amdgcn_fence(__ATOMIC_RELEASE, "agent");
;             asm volatile("s_waitcnt vmcnt(0)" ::: "memory");
;             const unsigned og = xb_add(&bar[XB_TOP], 1u);
;             const unsigned tg = og / nx;
;             if (og + 1u == (tg + 1u) * nx) xb_add(&bar[XB_TOPGEN], 1u);
;             else XB_SPIN(xb_ld(&bar[XB_TOPGEN]) == tg, bar);
;             __builtin_amdgcn_fence(__ATOMIC_ACQUIRE, "agent");
;             xb_add(&bar[XB_XGEN(bx)], 1u);
.LBB0_903:
	s_mov_b32 s0, s93
	s_waitcnt vmcnt(0) lgkmcnt(0)
	s_barrier
	s_waitcnt vmcnt(0)
	s_barrier
	s_nop 0
	v_mbcnt_lo_u32_b32 v0, -1, s0
	v_mbcnt_hi_u32_b32 v0, -1, v0
	v_readlane_b32 s0, v254, 17
	s_nop 1
	v_cmp_eq_u32_e32 vcc, s0, v0
	s_and_saveexec_b64 s[0:1], vcc
	s_cbranch_execz .LBB0_947
	s_bitcmp1_b32 s100, 0
	s_cbranch_scc0 .Lgb3_orig
	v_readlane_b32 s2, v253, 53
	v_readlane_b32 s3, v253, 54
	s_getreg_b32 s4, hwreg(HW_REG_XCC_ID, 0, 4)
	v_mov_b32_e32 v1, 1
	s_and_b32 s4, s4, 15
	s_lshl_b32 s4, s4, 8
	s_addk_i32 s4, 0x1400
	v_mov_b32_e32 v0, s4
	s_waitcnt vmcnt(0) lgkmcnt(0)
	global_atomic_add v2, v0, v1, s[2:3] sc0
	s_waitcnt vmcnt(0)
	v_readfirstlane_b32 s4, v2
	s_lshr_b32 s5, s4, 5
	s_and_b32 s4, s4, 31
	s_add_i32 s5, s5, 1
	s_lshl_b32 s5, s5, 3
	s_cmp_lg_u32 s4, 31
	s_cbranch_scc0 .Lgb3_last
	s_and_b32 s4, s4, 15
	s_cmp_lg_u32 s4, 0
	s_cbranch_scc1 .Lgb3_poll
	buffer_wbl2 sc1
	s_branch .Lgb3_poll
.Lgb3_last:
	buffer_wbl2 sc1
	s_waitcnt vmcnt(0)
	v_add_u32_e32 v0, 0x1000, v0
	global_atomic_add v0, v1, s[2:3]
	v_mov_b32_e32 v0, 0x3400
	global_atomic_add v2, v0, v1, s[2:3] sc0
	s_waitcnt vmcnt(0)
	v_readfirstlane_b32 s4, v2
	s_add_i32 s4, s4, 1
	s_cmp_lg_u32 s4, s5
	s_cbranch_scc1 .Lgb3_poll
	v_mov_b32_e32 v0, 0x3500
	global_atomic_add v0, v1, s[2:3]
	s_branch .Lgb3_done

; __device__ __forceinline__ unsigned xb_ld(unsigned* p)              { return __hip_atomic_load(p, __ATOMIC_RELAXED, __HIP_MEMORY_SCOPE_AGENT); }
; __device__ __forceinline__ unsigned xb_add(unsigned* p, unsigned v) { return __hip_atomic_fetch_add(p, v, __ATOMIC_RELAXED, __HIP_MEMORY_SCOPE_AGENT); }
; __device__ __forceinline__ unsigned xb_xcc_id() { return (unsigned)__builtin_amdgcn_s_getreg((3 << 11) | 20) & 0xFu; }
; #define XB_SPIN(cond, bar) do { unsigned _sp = 0; while (cond) { __builtin_amdgcn_s_sleep(1); \
;     if ((++_sp & 255u) == 0u) { if (xb_ld(&(bar)[XB_TMO])) break; if (_sp > XB_SPIN_CAP) { atomicAdd(&(bar)[XB_TMO], 1u); break; } } } } while (0)
; __device__ __forceinline__ void xcd_barrier(const XcdBarrier& b) {
;     ...
;         __builtin_amdgcn_s_waitcnt(0);
;         const unsigned bx = xb_xcc_id();
;         unsigned nloc = b.st[0], nx = b.st[1];
;         if (nloc == 0u) { xcd_barrier_complete(bar, bx, nloc, nx); b.st[0] = nloc; b.st[1] = nx; }
;         const unsigned old = xb_add(&bar[XB_XSUB(bx)], 1u);
;         const unsigned gen = old / nloc;
;         if (old + 1u == (gen + 1u) * nloc) {
;             __builtin_amdgcn_fence(__ATOMIC_RELEASE, "agent");
;             asm volatile("s_waitcnt vmcnt(0)" ::: "memory");
;             const unsigned og = xb_add(&bar[XB_TOP], 1u);
;             const unsigned tg = og / nx;
;             if (og + 1u == (tg + 1u) * nx) xb_add(&bar[XB_TOPGEN], 1u);
;             else XB_SPIN(xb_ld(&bar[XB_TOPGEN]) == tg, bar);
;             __builtin_amdgcn_fence(__ATOMIC_ACQUIRE, "agent");
;             xb_add(&bar[XB_XGEN(bx)], 1u);
.LBB0_1323:
	s_mov_b32 s0, s93
	s_waitcnt vmcnt(0)
	s_waitcnt lgkmcnt(0)
	s_barrier
	s_nop 0
	v_mbcnt_lo_u32_b32 v0, -1, s0
	v_mbcnt_hi_u32_b32 v0, -1, v0
	v_readlane_b32 s0, v254, 17
	s_nop 1
	v_cmp_eq_u32_e32 vcc, s0, v0
	s_and_saveexec_b64 s[0:1], vcc
	s_cbranch_execz .LBB0_1367
	s_bitcmp1_b32 s100, 0
	s_cbranch_scc0 .Lgb4_orig
	v_readlane_b32 s2, v253, 53
	v_readlane_b32 s3, v253, 54
	s_getreg_b32 s4, hwreg(HW_REG_XCC_ID, 0, 4)
	v_mov_b32_e32 v1, 1
	s_and_b32 s4, s4, 15
	s_lshl_b32 s4, s4, 8
	s_addk_i32 s4, 0x1400
	v_mov_b32_e32 v0, s4
	s_waitcnt vmcnt(0) lgkmcnt(0)
	global_atomic_add v2, v0, v1, s[2:3] sc0
	s_waitcnt vmcnt(0)
	v_readfirstlane_b32 s4, v2
	s_lshr_b32 s5, s4, 5
	s_and_b32 s4, s4, 31
	s_add_i32 s5, s5, 1
	s_lshl_b32 s5, s5, 3
	s_cmp_lg_u32 s4, 31
	s_cbranch_scc0 .Lgb4_last
	s_and_b32 s4, s4, 15
	s_cmp_lg_u32 s4, 0
	s_cbranch_scc1 .Lgb4_poll
	buffer_wbl2 sc1
	s_branch .Lgb4_poll

; __device__ __forceinline__ unsigned xb_ld(unsigned* p)              { return __hip_atomic_load(p, __ATOMIC_RELAXED, __HIP_MEMORY_SCOPE_AGENT); }
; __device__ __forceinline__ unsigned xb_add(unsigned* p, unsigned v) { return __hip_atomic_fetch_add(p, v, __ATOMIC_RELAXED, __HIP_MEMORY_SCOPE_AGENT); }
; __device__ __forceinline__ unsigned xb_xcc_id() { return (unsigned)__builtin_amdgcn_s_getreg((3 << 11) | 20) & 0xFu; }
; #define XB_SPIN(cond, bar) do { unsigned _sp = 0; while (cond) { __builtin_amdgcn_s_sleep(1); \
;     if ((++_sp & 255u) == 0u) { if (xb_ld(&(bar)[XB_TMO])) break; if (_sp > XB_SPIN_CAP) { atomicAdd(&(bar)[XB_TMO], 1u); break; } } } } while (0)
; __device__ __forceinline__ void xcd_barrier(const XcdBarrier& b) {
;     ...
;         __builtin_amdgcn_s_waitcnt(0);
;         const unsigned bx = xb_xcc_id();
;         unsigned nloc = b.st[0], nx = b.st[1];
;         if (nloc == 0u) { xcd_barrier_complete(bar, bx, nloc, nx); b.st[0] = nloc; b.st[1] = nx; }
;         const unsigned old = xb_add(&bar[XB_XSUB(bx)], 1u);
;         const unsigned gen = old / nloc;
;         if (old + 1u == (gen + 1u) * nloc) {
;             __builtin_amdgcn_fence(__ATOMIC_RELEASE, "agent");
;             asm volatile("s_waitcnt vmcnt(0)" ::: "memory");
;             const unsigned og = xb_add(&bar[XB_TOP], 1u);
;             const unsigned tg = og / nx;
;             if (og + 1u == (tg + 1u) * nx) xb_add(&bar[XB_TOPGEN], 1u);
;             else XB_SPIN(xb_ld(&bar[XB_TOPGEN]) == tg, bar);
;             __builtin_amdgcn_fence(__ATOMIC_ACQUIRE, "agent");
;             xb_add(&bar[XB_XGEN(bx)], 1u);
.LBB0_1402:
	s_mov_b32 s1, s93
	s_waitcnt vmcnt(0)
	s_waitcnt lgkmcnt(0)
	s_barrier
	s_nop 0
	v_mbcnt_lo_u32_b32 v0, -1, s1
	v_mbcnt_hi_u32_b32 v0, -1, v0
	v_readlane_b32 s1, v254, 17
	s_nop 1
	v_cmp_eq_u32_e32 vcc, s1, v0
	s_and_saveexec_b64 s[42:43], vcc
	s_mov_b32 s33, 0x42fe0000
	s_movk_i32 s60, 0x3800
	s_mov_b32 s61, 0xc0c0500
	s_mov_b32 s62, 0x43800000
	s_cbranch_execz .LBB0_1446
	s_bitcmp1_b32 s100, 0
	s_cbranch_scc0 .Lgb5_orig
	v_readlane_b32 s44, v253, 53
	v_readlane_b32 s45, v253, 54
	s_getreg_b32 s1, hwreg(HW_REG_XCC_ID, 0, 4)
	v_mov_b32_e32 v1, 1
	s_and_b32 s1, s1, 15
	s_lshl_b32 s1, s1, 8
	s_addk_i32 s1, 0x1400
	v_mov_b32_e32 v0, s1
	s_waitcnt vmcnt(0) lgkmcnt(0)
	global_atomic_add v2, v0, v1, s[44:45] sc0
	s_waitcnt vmcnt(0)
	v_readfirstlane_b32 s1, v2
	s_lshr_b32 s4, s1, 5
	s_and_b32 s1, s1, 31
	s_add_i32 s4, s4, 1
	s_lshl_b32 s4, s4, 3
	s_cmp_lg_u32 s1, 31
	s_cbranch_scc0 .Lgb5_last
	s_and_b32 s1, s1, 15
	s_cmp_lg_u32 s1, 0
	s_cbranch_scc1 .Lgb5_poll
	buffer_wbl2 sc1
	s_branch .Lgb5_poll
.Lgb5_last:
	buffer_wbl2 sc1
	s_waitcnt vmcnt(0)
	v_add_u32_e32 v0, 0x1000, v0
	global_atomic_add v0, v1, s[44:45]
	v_mov_b32_e32 v0, 0x3400
	global_atomic_add v2, v0, v1, s[44:45] sc0
	s_waitcnt vmcnt(0)
	v_readfirstlane_b32 s1, v2
	s_add_i32 s1, s1, 1
	s_cmp_lg_u32 s1, s4
	s_cbranch_scc1 .Lgb5_poll
	v_mov_b32_e32 v0, 0x3500
	global_atomic_add v0, v1, s[44:45]
	s_branch .Lgb5_done

; __device__ __forceinline__ unsigned xb_ld(unsigned* p)              { return __hip_atomic_load(p, __ATOMIC_RELAXED, __HIP_MEMORY_SCOPE_AGENT); }
; __device__ __forceinline__ unsigned xb_add(unsigned* p, unsigned v) { return __hip_atomic_fetch_add(p, v, __ATOMIC_RELAXED, __HIP_MEMORY_SCOPE_AGENT); }
; __device__ __forceinline__ unsigned xb_xcc_id() { return (unsigned)__builtin_amdgcn_s_getreg((3 << 11) | 20) & 0xFu; }
; #define XB_SPIN(cond, bar) do { unsigned _sp = 0; while (cond) { __builtin_amdgcn_s_sleep(1); \
;     if ((++_sp & 255u) == 0u) { if (xb_ld(&(bar)[XB_TMO])) break; if (_sp > XB_SPIN_CAP) { atomicAdd(&(bar)[XB_TMO], 1u); break; } } } } while (0)
; __device__ __forceinline__ void xcd_barrier(const XcdBarrier& b) {
;     ...
;         __builtin_amdgcn_s_waitcnt(0);
;         const unsigned bx = xb_xcc_id();
;         unsigned nloc = b.st[0], nx = b.st[1];
;         if (nloc == 0u) { xcd_barrier_complete(bar, bx, nloc, nx); b.st[0] = nloc; b.st[1] = nx; }
;         const unsigned old = xb_add(&bar[XB_XSUB(bx)], 1u);
;         const unsigned gen = old / nloc;
;         if (old + 1u == (gen + 1u) * nloc) {
;             __builtin_amdgcn_fence(__ATOMIC_RELEASE, "agent");
;             asm volatile("s_waitcnt vmcnt(0)" ::: "memory");
;             const unsigned og = xb_add(&bar[XB_TOP], 1u);
;             const unsigned tg = og / nx;
;             if (og + 1u == (tg + 1u) * nx) xb_add(&bar[XB_TOPGEN], 1u);
;             else XB_SPIN(xb_ld(&bar[XB_TOPGEN]) == tg, bar);
;             __builtin_amdgcn_fence(__ATOMIC_ACQUIRE, "agent");
;             xb_add(&bar[XB_XGEN(bx)], 1u);
.LBB0_1472:
	s_mov_b32 s0, s93
	s_waitcnt vmcnt(0)
	s_waitcnt lgkmcnt(0)
	s_barrier
	s_nop 0
	v_mbcnt_lo_u32_b32 v0, -1, s0
	v_mbcnt_hi_u32_b32 v0, -1, v0
	v_readlane_b32 s0, v254, 17
	s_nop 1
	v_cmp_eq_u32_e32 vcc, s0, v0
	s_and_saveexec_b64 s[0:1], vcc
	s_cbranch_execz .LBB0_1516
	s_bitcmp1_b32 s100, 0
	s_cbranch_scc0 .Lgb6_orig
	v_readlane_b32 s34, v253, 53
	v_readlane_b32 s35, v253, 54
	s_getreg_b32 s2, hwreg(HW_REG_XCC_ID, 0, 4)
	v_mov_b32_e32 v1, 1
	s_and_b32 s2, s2, 15
	s_lshl_b32 s2, s2, 8
	s_addk_i32 s2, 0x1400
	v_mov_b32_e32 v0, s2
	s_waitcnt vmcnt(0) lgkmcnt(0)
	global_atomic_add v2, v0, v1, s[34:35] sc0
	s_waitcnt vmcnt(0)
	v_readfirstlane_b32 s2, v2
	s_lshr_b32 s3, s2, 5
	s_and_b32 s2, s2, 31
	s_add_i32 s3, s3, 1
	s_lshl_b32 s3, s3, 3
	s_cmp_lg_u32 s2, 31
	s_cbranch_scc0 .Lgb6_last
	s_and_b32 s2, s2, 15
	s_cmp_lg_u32 s2, 0
	s_cbranch_scc1 .Lgb6_poll
	buffer_wbl2 sc1
	s_branch .Lgb6_poll
.Lgb6_last:
	buffer_wbl2 sc1
	s_waitcnt vmcnt(0)
	v_add_u32_e32 v0, 0x1000, v0
	global_atomic_add v0, v1, s[34:35]
	v_mov_b32_e32 v0, 0x3400
	global_atomic_add v2, v0, v1, s[34:35] sc0
	s_waitcnt vmcnt(0)
	v_readfirstlane_b32 s2, v2
	s_add_i32 s2, s2, 1
	s_cmp_lg_u32 s2, s3
	s_cbranch_scc1 .Lgb6_poll
	v_mov_b32_e32 v0, 0x3500
	global_atomic_add v0, v1, s[34:35]
	s_branch .Lgb6_done

; __device__ __forceinline__ unsigned xb_ld(unsigned* p)              { return __hip_atomic_load(p, __ATOMIC_RELAXED, __HIP_MEMORY_SCOPE_AGENT); }
; __device__ __forceinline__ unsigned xb_add(unsigned* p, unsigned v) { return __hip_atomic_fetch_add(p, v, __ATOMIC_RELAXED, __HIP_MEMORY_SCOPE_AGENT); }
; __device__ __forceinline__ unsigned xb_xcc_id() { return (unsigned)__builtin_amdgcn_s_getreg((3 << 11) | 20) & 0xFu; }
; #define XB_SPIN(cond, bar) do { unsigned _sp = 0; while (cond) { __builtin_amdgcn_s_sleep(1); \
;     if ((++_sp & 255u) == 0u) { if (xb_ld(&(bar)[XB_TMO])) break; if (_sp > XB_SPIN_CAP) { atomicAdd(&(bar)[XB_TMO], 1u); break; } } } } while (0)
; __device__ __forceinline__ void xcd_barrier(const XcdBarrier& b) {
;     ...
;         __builtin_amdgcn_s_waitcnt(0);
;         const unsigned bx = xb_xcc_id();
;         unsigned nloc = b.st[0], nx = b.st[1];
;         if (nloc == 0u) { xcd_barrier_complete(bar, bx, nloc, nx); b.st[0] = nloc; b.st[1] = nx; }
;         const unsigned old = xb_add(&bar[XB_XSUB(bx)], 1u);
;         const unsigned gen = old / nloc;
;         if (old + 1u == (gen + 1u) * nloc) {
;             __builtin_amdgcn_fence(__ATOMIC_RELEASE, "agent");
;             asm volatile("s_waitcnt vmcnt(0)" ::: "memory");
;             const unsigned og = xb_add(&bar[XB_TOP], 1u);
;             const unsigned tg = og / nx;
;             if (og + 1u == (tg + 1u) * nx) xb_add(&bar[XB_TOPGEN], 1u);
;             else XB_SPIN(xb_ld(&bar[XB_TOPGEN]) == tg, bar);
;             __builtin_amdgcn_fence(__ATOMIC_ACQUIRE, "agent");
;             xb_add(&bar[XB_XGEN(bx)], 1u);
.LBB0_1569:
	s_mov_b32 s0, s93
	s_waitcnt vmcnt(0)
	s_waitcnt lgkmcnt(0)
	s_barrier
	s_nop 0
	v_mbcnt_lo_u32_b32 v0, -1, s0
	v_mbcnt_hi_u32_b32 v0, -1, v0
	v_readlane_b32 s0, v254, 17
	s_nop 1
	v_cmp_eq_u32_e32 vcc, s0, v0
	s_and_saveexec_b64 s[0:1], vcc
	s_cbranch_execz .LBB0_1613
	s_bitcmp1_b32 s100, 0
	s_cbranch_scc0 .Lgb7_orig
	v_readlane_b32 s64, v253, 53
	v_readlane_b32 s65, v253, 54
	s_getreg_b32 s2, hwreg(HW_REG_XCC_ID, 0, 4)
	v_mov_b32_e32 v1, 1
	s_and_b32 s2, s2, 15
	s_lshl_b32 s2, s2, 8
	s_addk_i32 s2, 0x1400
	v_mov_b32_e32 v0, s2
	s_waitcnt vmcnt(0) lgkmcnt(0)
	global_atomic_add v2, v0, v1, s[64:65] sc0
	s_waitcnt vmcnt(0)
	v_readfirstlane_b32 s2, v2
	s_lshr_b32 s3, s2, 5
	s_and_b32 s2, s2, 31
	s_add_i32 s3, s3, 1
	s_lshl_b32 s3, s3, 3
	s_cmp_lg_u32 s2, 31
	s_cbranch_scc0 .Lgb7_last
	s_and_b32 s2, s2, 15
	s_cmp_lg_u32 s2, 0
	s_cbranch_scc1 .Lgb7_poll
	buffer_wbl2 sc1
	s_branch .Lgb7_poll
.Lgb7_last:
	buffer_wbl2 sc1
	s_waitcnt vmcnt(0)
	v_add_u32_e32 v0, 0x1000, v0
	global_atomic_add v0, v1, s[64:65]
	v_mov_b32_e32 v0, 0x3400
	global_atomic_add v2, v0, v1, s[64:65] sc0
	s_waitcnt vmcnt(0)
	v_readfirstlane_b32 s2, v2
	s_add_i32 s2, s2, 1
	s_cmp_lg_u32 s2, s3
	s_cbranch_scc1 .Lgb7_poll
	v_mov_b32_e32 v0, 0x3500
	global_atomic_add v0, v1, s[64:65]
	s_branch .Lgb7_done

; __device__ __forceinline__ unsigned xb_ld(unsigned* p)              { return __hip_atomic_load(p, __ATOMIC_RELAXED, __HIP_MEMORY_SCOPE_AGENT); }
; __device__ __forceinline__ unsigned xb_add(unsigned* p, unsigned v) { return __hip_atomic_fetch_add(p, v, __ATOMIC_RELAXED, __HIP_MEMORY_SCOPE_AGENT); }
; __device__ __forceinline__ unsigned xb_xcc_id() { return (unsigned)__builtin_amdgcn_s_getreg((3 << 11) | 20) & 0xFu; }
; #define XB_SPIN(cond, bar) do { unsigned _sp = 0; while (cond) { __builtin_amdgcn_s_sleep(1); \
;     if ((++_sp & 255u) == 0u) { if (xb_ld(&(bar)[XB_TMO])) break; if (_sp > XB_SPIN_CAP) { atomicAdd(&(bar)[XB_TMO], 1u); break; } } } } while (0)
; __device__ __forceinline__ void xcd_barrier(const XcdBarrier& b) {
;     ...
;         __builtin_amdgcn_s_waitcnt(0);
;         const unsigned bx = xb_xcc_id();
;         unsigned nloc = b.st[0], nx = b.st[1];
;         if (nloc == 0u) { xcd_barrier_complete(bar, bx, nloc, nx); b.st[0] = nloc; b.st[1] = nx; }
;         const unsigned old = xb_add(&bar[XB_XSUB(bx)], 1u);
;         const unsigned gen = old / nloc;
;         if (old + 1u == (gen + 1u) * nloc) {
;             __builtin_amdgcn_fence(__ATOMIC_RELEASE, "agent");
;             asm volatile("s_waitcnt vmcnt(0)" ::: "memory");
;             const unsigned og = xb_add(&bar[XB_TOP], 1u);
;             const unsigned tg = og / nx;
;             if (og + 1u == (tg + 1u) * nx) xb_add(&bar[XB_TOPGEN], 1u);
;             else XB_SPIN(xb_ld(&bar[XB_TOPGEN]) == tg, bar);
;             __builtin_amdgcn_fence(__ATOMIC_ACQUIRE, "agent");
;             xb_add(&bar[XB_XGEN(bx)], 1u);
.LBB0_1714:
	s_mov_b32 s0, s93
	s_waitcnt vmcnt(0)
	s_waitcnt lgkmcnt(0)
	s_barrier
	s_nop 0
	v_mbcnt_lo_u32_b32 v0, -1, s0
	v_mbcnt_hi_u32_b32 v0, -1, v0
	v_readlane_b32 s0, v254, 17
	s_nop 1
	v_cmp_eq_u32_e32 vcc, s0, v0
	s_and_saveexec_b64 s[38:39], vcc
	s_cbranch_execz .LBB0_1758
	s_bitcmp1_b32 s100, 0
	s_cbranch_scc0 .Lgb9_orig
	v_readlane_b32 s40, v253, 53
	v_readlane_b32 s41, v253, 54
	s_getreg_b32 s0, hwreg(HW_REG_XCC_ID, 0, 4)
	v_mov_b32_e32 v1, 1
	s_and_b32 s0, s0, 15
	s_lshl_b32 s0, s0, 8
	s_addk_i32 s0, 0x1400
	v_mov_b32_e32 v0, s0
	s_waitcnt vmcnt(0) lgkmcnt(0)
	global_atomic_add v2, v0, v1, s[40:41] sc0
	s_waitcnt vmcnt(0)
	v_readfirstlane_b32 s0, v2
	s_lshr_b32 s1, s0, 5
	s_and_b32 s0, s0, 31
	s_add_i32 s1, s1, 1
	s_lshl_b32 s1, s1, 3
	s_cmp_lg_u32 s0, 31
	s_cbranch_scc0 .Lgb9_last
	s_and_b32 s0, s0, 15
	s_cmp_lg_u32 s0, 0
	s_cbranch_scc1 .Lgb9_poll
	buffer_wbl2 sc1
	s_branch .Lgb9_poll
